# window attention unit prologue: compiler vmcnt(0) before the first tile's QK dropped (only lgkmcnt(0) kept); the K1/V0/conversion DMAs keep their explicit waits before the publishing barrier
# speedup vs baseline: 1.0084x; 1.0017x over previous
.LBB0_1966:
	v_lshrrev_b32_e32 v2, 5, v179
	v_lshlrev_b32_e32 v3, 7, v185
	v_bitop3_b32 v4, v2, v186, 1 bitop3:0x78
	v_lshlrev_b32_e32 v88, 3, v185
	v_lshlrev_b32_e32 v187, 2, v2
	v_and_b32_e32 v2, 0xf80, v3
	v_and_b32_e32 v6, 0x60, v88
	v_lshl_or_b32 v7, v4, 4, v2
	v_or_b32_e32 v190, v7, v6
	v_add_u32_e32 v194, 0, v190
	ds_read_b128 v[2:5], v194
	v_bitop3_b32 v191, v7, 32, v6 bitop3:0x36
	v_add_u32_e32 v195, 0, v191
	v_bitop3_b32 v192, v7, 64, v6 bitop3:0x36
	v_add_u32_e32 v196, 0, v192
	s_movk_i32 s2, 0x60
	v_bitop3_b32 v193, v7, s2, v88 bitop3:0x34
	v_add_u32_e32 v197, 0, v193
	s_cmp_lt_i32 s87, 1
	s_waitcnt lgkmcnt(0)
	v_mfma_f32_32x32x16_bf16 v[50:65], v[2:5], v[82:85], 0
	ds_read_b128 v[2:5], v194 offset:4096
	s_waitcnt lgkmcnt(0)
	v_mfma_f32_32x32x16_bf16 v[66:81], v[2:5], v[82:85], 0
	ds_read_b128 v[2:5], v195
	s_waitcnt lgkmcnt(0)
	v_mfma_f32_32x32x16_bf16 v[50:65], v[2:5], v[140:143], v[50:65]
	ds_read_b128 v[2:5], v195 offset:4096
	s_waitcnt lgkmcnt(0)
	v_mfma_f32_32x32x16_bf16 v[66:81], v[2:5], v[140:143], v[66:81]
	ds_read_b128 v[2:5], v196
	s_waitcnt lgkmcnt(0)
	v_mfma_f32_32x32x16_bf16 v[50:65], v[2:5], v[136:139], v[50:65]
	ds_read_b128 v[2:5], v196 offset:4096
	s_waitcnt lgkmcnt(0)
	v_mfma_f32_32x32x16_bf16 v[66:81], v[2:5], v[136:139], v[66:81]
	ds_read_b128 v[2:5], v197
	s_waitcnt lgkmcnt(0)
	v_mfma_f32_32x32x16_bf16 v[50:65], v[2:5], v[132:135], v[50:65]
	ds_read_b128 v[2:5], v197 offset:4096
	s_waitcnt lgkmcnt(0)
	v_mfma_f32_32x32x16_bf16 v[66:81], v[2:5], v[132:135], v[66:81]
	s_cbranch_scc1 .LBB0_1971
	s_sub_i32 s2, s86, s89
	s_add_i32 s2, s2, 63
	s_cmpk_gt_i32 s2, 0x80
	s_cselect_b64 s[38:39], -1, 0
	s_and_b64 vcc, exec, s[38:39]
	s_cbranch_vccnz .LBB0_1969
	s_sub_i32 s2, s89, s86
	s_add_i32 s2, s2, 31
	s_cmpk_gt_i32 s2, 0x80
	s_cselect_b64 s[38:39], -1, 0
